# prologue Fourier-weight fold scheduled per SIMD (waves 0-3 fold in round 0, waves 4-7 in round 1) now that only few static conversion rounds remain
# speedup vs baseline: 1.0000x; 1.0000x over previous
.LBB0_41:
	v_writelane_b32 v253, s24, 32
	v_writelane_b32 v253, s23, 34
	v_writelane_b32 v253, s22, 36
	s_mov_b32 s3, 0
	v_readlane_b32 s0, v253, 29
	s_lshl_b32 s0, s0, 14
	s_add_i32 s29, s0, 0
	s_cmp_lg_u64 s[48:49], 0
	v_readlane_b32 s4, v253, 30
	s_cselect_b64 s[44:45], -1, 0
	s_abs_i32 s2, s4
	v_cvt_f32_u32_e32 v2, s2
	s_sub_i32 s0, 0, s2
	s_ashr_i32 s6, s4, 31
	v_rcp_iflag_f32_e32 v2, v2
	s_nop 0
	v_mul_f32_e32 v2, 0x4f7ffffe, v2
	v_cvt_u32_f32_e32 v2, v2
	s_nop 0
	v_readfirstlane_b32 s1, v2
	s_mul_i32 s0, s0, s1
	s_mul_hi_u32 s0, s1, s0
	s_add_i32 s7, s1, s0
	s_mul_hi_u32 s0, s7, 0x4200
	s_mul_i32 s0, s0, s2
	s_sub_i32 s0, 0x4200, s0
	s_sub_i32 s1, s0, s2
	s_cmp_ge_u32 s0, s2
	s_cselect_b32 s0, s1, s0
	s_sub_i32 s1, s0, s2
	s_cmp_ge_u32 s0, s2
	s_cselect_b32 s8, s1, s0
	s_add_i32 s0, s4, 0xffffff00
	s_cmp_ge_i32 s0, s8
	s_cselect_b64 s[0:1], -1, 0
	s_cmpk_lt_u32 s8, 0x2101
	s_cselect_b64 s[4:5], -1, 0
	s_sub_i32 s8, 0x4200, s8
	s_and_b64 s[0:1], s[0:1], s[4:5]
	s_and_b64 s[0:1], s[0:1], exec
	s_cselect_b32 s5, s8, 0x4200
	s_add_i32 s0, s5, 0xffffd200
	s_cmp_eq_u32 s2, 0x800
	s_cselect_b32 s5, s0, s5
	v_writelane_b32 v253, s5, 38
	v_writelane_b32 v253, s48, 40
	s_mul_hi_u32 s0, s5, s7
	s_mul_i32 s1, s0, s2
	v_writelane_b32 v253, s49, 41
	v_writelane_b32 v253, s50, 42
	v_writelane_b32 v253, s51, 43
	v_writelane_b32 v253, s52, 44
	v_writelane_b32 v253, s53, 45
	v_writelane_b32 v253, s54, 46
	v_writelane_b32 v253, s55, 47
	s_sub_i32 s1, s5, s1
	v_writelane_b32 v253, s56, 48
	s_add_i32 s4, s0, 1
	s_sub_i32 s5, s1, s2
	v_writelane_b32 v253, s57, 49
	s_cmp_ge_u32 s1, s2
	v_writelane_b32 v253, s58, 50
	s_cselect_b32 s0, s4, s0
	v_writelane_b32 v253, s59, 51
	s_cselect_b32 s1, s5, s1
	s_add_i32 s4, s0, 1
	v_writelane_b32 v253, s60, 52
	s_cmp_ge_u32 s1, s2
	v_writelane_b32 v253, s61, 53
	s_cselect_b32 s0, s4, s0
	v_writelane_b32 v253, s62, 54
	s_xor_b32 s0, s0, s6
	v_writelane_b32 v253, s63, 55
	s_sub_i32 s15, s0, s6
	v_writelane_b32 v253, s29, 56
	s_add_i32 s14, s15, -1
	v_writelane_b32 v253, s44, 57
	s_cmp_lt_i32 s15, 1
	v_readfirstlane_b32 s0, v0
	v_writelane_b32 v253, s45, 58
	s_cbranch_scc1 .LBB0_65
	s_ashr_i32 s0, s0, 8
	s_min_i32 s18, s0, s14
	s_cmpk_gt_i32 s27, 0x7ff
	v_readlane_b32 s0, v253, 26
	s_cselect_b64 s[20:21], -1, 0
	s_add_u32 s0, s0, 0x800000
	v_writelane_b32 v253, s0, 59
	v_mov_b32_e32 v133, 0
	v_readlane_b32 s0, v253, 27
	s_addc_u32 s0, s0, 0
	s_add_i32 s25, 0, 0x21000
	v_writelane_b32 v253, s0, 61
	s_add_i32 s0, 0, 0x21200
	v_writelane_b32 v253, s0, 63
	s_add_i32 s0, 0, 0x21100
	v_writelane_b32 v254, s0, 1
	s_add_i32 s0, 0, 0x21300
	v_writelane_b32 v254, s0, 3
	v_writelane_b32 v254, s27, 5
	v_writelane_b32 v254, s14, 7
	v_writelane_b32 v254, s15, 9
	v_writelane_b32 v254, s18, 11
	v_writelane_b32 v254, s20, 13
	s_mov_b32 s22, 0x42800000
	s_mov_b32 s19, 0
	v_writelane_b32 v254, s21, 14
	s_branch .LBB0_45
